# code placement: every 8-byte instruction of the latent attention tile loop placed on an 8-byte boundary (e32 VALU ops re-encoded as VOP3 or s_nop pads)
# baseline (speedup 1.0000x reference)
.LBB0_439:
	s_add_i32 s25, s26, 1
	s_and_b32 s27, s26, 1
	s_mul_i32 s24, s27, 0x4400
	s_mul_i32 s31, s27, 0x4800
	v_add_u32_e32 v12, s24, v0
	v_add_u32_e32 v14, s31, v1
	ds_read_b128 v[228:231], v12 offset:0
	ds_read_b128 v[232:235], v12 offset:32
	ds_read_b128 v[236:239], v12 offset:64
	ds_read_b128 v[240:243], v12 offset:96
	ds_read_b128 v[244:247], v13 offset:0
	ds_read_b128 v[248:251], v13 offset:32
	ds_read_b128 v[4:7], v13 offset:64
	ds_read_b128 v[8:11], v13 offset:96
	ds_read_b128 v[184:187], v14 offset:34816
	ds_read_b128 v[188:191], v14 offset:39424
	ds_read_b128 v[192:195], v14 offset:44032
	ds_read_b128 v[196:199], v14 offset:48640
	ds_read_b128 v[200:203], v14 offset:34848
	ds_read_b128 v[212:215], v14 offset:39456
	ds_read_b128 v[216:219], v14 offset:44064
	s_cmpk_gt_u32 s26, 0x42
	s_cbranch_scc1 .Lat_noload
	s_cmp_lt_u32 s26, 3
	s_cselect_b32 s24, s22, s21
	s_cselect_b32 s31, s13, s15
	s_add_i32 s24, s24, s23
	v_and_b32_e32 v15, 63, v204
	v_ashrrev_i32_e32 v227, 6, v204
	v_add_u32_e32 v211, s24, v15
	v_lshlrev_b32_e64 v227, 4, v227
	s_add_i32 s31, s31, s14
	v_mul_u32_u24_e32 v211, 0x1400, v211
	s_add_i32 s31, s31, s23
	s_add_i32 s31, s31, 64
	v_add_u32_e64 v211, v211, v227
	s_mul_hi_i32 s37, s31, 0x1400
	s_mul_i32 s36, s31, 0x1400
	v_lshlrev_b32_e64 v15, 2, v15
	global_load_dwordx4 v[176:179], v211, s[2:3] offset:2048
	global_load_dwordx4 v[180:183], v211, s[2:3] offset:2176
	s_add_u32 s36, s2, s36
	s_addc_u32 s37, s3, s37
	v_readfirstlane_b32 s38, v205
	s_xor_b32 s39, s27, 1
	v_add_u32_e32 v15, 0x400, v15
	s_mul_i32 s39, s39, 0x4400
	s_add_i32 s38, s38, s19
	s_add_i32 s38, s38, s39
	s_add_i32 m0, s38, 0
	s_nop 0
	global_load_lds_dword v15, s[36:37]
	s_add_u32 s36, s36, 0x1400
	s_addc_u32 s37, s37, 0
	s_nop 0
	s_add_i32 m0, s38, 272
	s_nop 0
	s_nop 0
	global_load_lds_dword v15, s[36:37]
	s_add_u32 s36, s36, 0x1400
	s_addc_u32 s37, s37, 0
	s_nop 0
	s_add_i32 m0, s38, 544
	s_nop 0
	s_nop 0
	global_load_lds_dword v15, s[36:37]
	s_add_u32 s36, s36, 0x1400
	s_addc_u32 s37, s37, 0
	s_nop 0
	s_add_i32 m0, s38, 816
	s_nop 0
	s_nop 0
	global_load_lds_dword v15, s[36:37]
	s_add_u32 s36, s36, 0x1400
	s_addc_u32 s37, s37, 0
	s_nop 0
	s_add_i32 m0, s38, 1088
	s_nop 0
	s_nop 0
	global_load_lds_dword v15, s[36:37]
	s_add_u32 s36, s36, 0x1400
	s_addc_u32 s37, s37, 0
	s_nop 0
	s_add_i32 m0, s38, 1360
	s_nop 0
	s_nop 0
	global_load_lds_dword v15, s[36:37]
	s_add_u32 s36, s36, 0x1400
	s_addc_u32 s37, s37, 0
	s_nop 0
	s_add_i32 m0, s38, 1632
	s_nop 0
	s_nop 0
	global_load_lds_dword v15, s[36:37]
	s_add_u32 s36, s36, 0x1400
	s_addc_u32 s37, s37, 0
	s_nop 0
	s_add_i32 m0, s38, 1904
	s_nop 0
	s_nop 0
	global_load_lds_dword v15, s[36:37]
.Lat_noload:
	s_waitcnt lgkmcnt(7)
	s_nop 0
	ds_read_b128 v[220:223], v14 offset:48672
	v_mfma_f32_32x32x16_bf16 v[144:159], v[228:231], v[244:247], 0
	v_mfma_f32_32x32x16_bf16 v[144:159], v[232:235], v[248:251], v[144:159]
	v_mfma_f32_32x32x16_bf16 v[144:159], v[236:239], v[4:7], v[144:159]
	v_mfma_f32_32x32x16_bf16 v[144:159], v[240:243], v[8:11], v[144:159]
	s_waitcnt lgkmcnt(0)
	s_nop 0
	ds_read_b128 v[228:231], v12 offset:128
	ds_read_b128 v[232:235], v12 offset:160
	ds_read_b128 v[236:239], v12 offset:192
	ds_read_b128 v[240:243], v12 offset:224
	ds_read_b128 v[244:247], v13 offset:128
	ds_read_b128 v[248:251], v13 offset:160
	ds_read_b128 v[4:7], v13 offset:192
	ds_read_b128 v[8:11], v13 offset:224
	s_nop 3
	s_nop 0
	v_max3_f32 v15, v144, v145, v146
	v_max3_f32 v211, v147, v148, v149
	v_max3_f32 v224, v150, v151, v152
	v_max3_f32 v225, v153, v154, v155
	v_max3_f32 v227, v156, v157, v158
	v_max3_f32 v15, v15, v211, v159
	v_max3_f32 v224, v224, v225, v227
	v_max_f32_e32 v15, v15, v224
	v_mov_b32_e32 v211, v15
	v_add_f32_e32 v225, 0x41000000, v209
	s_nop 1
	v_permlane32_swap_b32_e32 v15, v211
	v_max_f32_e32 v15, v15, v211
	v_cmp_gt_f32_e32 vcc, v15, v225
	s_cbranch_vccnz .Lat_slow0_s0
.Lat_back0_s0:
	v_sub_f32_e32 v144, v144, v209
	v_sub_f32_e32 v145, v145, v209
	v_sub_f32_e32 v146, v146, v209
	v_sub_f32_e32 v147, v147, v209
	v_exp_f32_e32 v144, v144
	v_exp_f32_e32 v145, v145
	v_exp_f32_e32 v146, v146
	v_exp_f32_e32 v147, v147
	v_sub_f32_e32 v148, v148, v209
	v_sub_f32_e32 v149, v149, v209
	v_sub_f32_e32 v150, v150, v209
	v_sub_f32_e32 v151, v151, v209
	v_exp_f32_e32 v148, v148
	v_exp_f32_e32 v149, v149
	v_exp_f32_e32 v150, v150
	v_exp_f32_e32 v151, v151
	s_waitcnt lgkmcnt(0)
	v_mfma_f32_32x32x16_bf16 v[160:175], v[228:231], v[244:247], 0
	v_sub_f32_e32 v152, v152, v209
	v_sub_f32_e32 v153, v153, v209
	v_sub_f32_e32 v154, v154, v209
	v_sub_f32_e32 v155, v155, v209
	v_exp_f32_e32 v152, v152
	v_exp_f32_e32 v153, v153
	v_exp_f32_e64 v154, v154
	v_mfma_f32_32x32x16_bf16 v[160:175], v[232:235], v[248:251], v[160:175]
	v_exp_f32_e32 v155, v155
	v_sub_f32_e32 v156, v156, v209
	v_sub_f32_e32 v157, v157, v209
	v_sub_f32_e32 v158, v158, v209
	v_sub_f32_e32 v159, v159, v209
	v_exp_f32_e32 v156, v156
	v_exp_f32_e64 v157, v157
	v_mfma_f32_32x32x16_bf16 v[160:175], v[236:239], v[4:7], v[160:175]
	v_exp_f32_e32 v158, v158
	v_exp_f32_e32 v159, v159
	v_add_f32_e32 v15, v144, v145
	v_add_f32_e32 v211, v146, v147
	v_add_f32_e32 v15, v15, v211
	v_add_f32_e32 v211, v148, v149
	v_add_f32_e32 v224, v150, v151
	v_add_f32_e32 v211, v211, v224
	v_add_f32_e32 v224, v152, v153
	v_add_f32_e32 v225, v154, v155
	v_mfma_f32_32x32x16_bf16 v[160:175], v[240:243], v[8:11], v[160:175]
	v_add_f32_e32 v224, v224, v225
	v_add_f32_e32 v225, v156, v157
	v_add_f32_e32 v227, v158, v159
	v_add_f32_e32 v225, v225, v227
	v_add_f32_e32 v15, v15, v211
	v_add_f32_e32 v224, v224, v225
	v_add_f32_e32 v15, v15, v224
	v_add_f32_e32 v210, v210, v15
	v_cvt_pk_bf16_f32 v144, v144, v145
	v_cvt_pk_bf16_f32 v145, v146, v147
	v_cvt_pk_bf16_f32 v146, v148, v149
	v_cvt_pk_bf16_f32 v147, v150, v151
	v_cvt_pk_bf16_f32 v148, v152, v153
	v_cvt_pk_bf16_f32 v149, v154, v155
	v_cvt_pk_bf16_f32 v150, v156, v157
	v_cvt_pk_bf16_f32 v151, v158, v159
	s_nop 1
	s_nop 0
	v_mfma_f32_32x32x16_bf16 v[128:143], v[184:187], v[144:147], v[128:143]
	ds_read_b128 v[228:231], v12 offset:8704
	ds_read_b128 v[232:235], v12 offset:8736
	ds_read_b128 v[236:239], v12 offset:8768
	ds_read_b128 v[240:243], v12 offset:8800
	ds_read_b128 v[244:247], v13 offset:0
	ds_read_b128 v[248:251], v13 offset:32
	ds_read_b128 v[4:7], v13 offset:64
	ds_read_b128 v[8:11], v13 offset:96
	v_max3_f32 v15, v160, v161, v162
	v_max3_f32 v211, v163, v164, v165
	v_max3_f32 v224, v166, v167, v168
	v_max3_f32 v225, v169, v170, v171
	v_mfma_f32_32x32x16_bf16 v[96:111], v[188:191], v[144:147], v[96:111]
	v_max3_f32 v227, v172, v173, v174
	v_max3_f32 v15, v15, v211, v175
	v_max3_f32 v224, v224, v225, v227
	v_max_f32_e32 v15, v15, v224
	v_mov_b32_e32 v211, v15
	v_add_f32_e32 v225, 0x41000000, v208
	s_nop 1
	v_permlane32_swap_b32_e32 v15, v211
	v_max_f32_e32 v15, v15, v211
	v_cmp_gt_f32_e32 vcc, v15, v225
	s_cbranch_vccnz .Lat_slow1_s0
.Lat_back1_s0:
	v_sub_f32_e32 v160, v160, v208
	v_mfma_f32_32x32x16_bf16 v[64:79], v[192:195], v[144:147], v[64:79]
	v_sub_f32_e32 v161, v161, v208
	v_sub_f32_e32 v162, v162, v208
	v_sub_f32_e32 v163, v163, v208
	v_exp_f32_e32 v160, v160
	v_exp_f32_e32 v161, v161
	v_exp_f32_e32 v162, v162
	v_mfma_f32_32x32x16_bf16 v[32:47], v[196:199], v[144:147], v[32:47]
	v_exp_f32_e32 v163, v163
	v_sub_f32_e32 v164, v164, v208
	v_sub_f32_e32 v165, v165, v208
	v_sub_f32_e32 v166, v166, v208
	v_sub_f32_e32 v167, v167, v208
	v_exp_f32_e32 v164, v164
	v_mfma_f32_32x32x16_bf16 v[128:143], v[200:203], v[148:151], v[128:143]
	v_exp_f32_e32 v165, v165
	v_exp_f32_e32 v166, v166
	v_exp_f32_e64 v167, v167
	v_mfma_f32_32x32x16_bf16 v[96:111], v[212:215], v[148:151], v[96:111]
	v_sub_f32_e32 v168, v168, v208
	v_sub_f32_e32 v169, v169, v208
	v_sub_f32_e32 v170, v170, v208
	v_sub_f32_e32 v171, v171, v208
	v_exp_f32_e32 v168, v168
	v_exp_f32_e32 v169, v169
	v_mfma_f32_32x32x16_bf16 v[64:79], v[216:219], v[148:151], v[64:79]
	v_exp_f32_e32 v170, v170
	v_exp_f32_e32 v171, v171
	v_sub_f32_e64 v172, v172, v208
	v_mfma_f32_32x32x16_bf16 v[32:47], v[220:223], v[148:151], v[32:47]
	v_sub_f32_e32 v173, v173, v208
	v_sub_f32_e32 v174, v174, v208
	v_sub_f32_e32 v175, v175, v208
	v_exp_f32_e32 v172, v172
	v_exp_f32_e32 v173, v173
	s_waitcnt lgkmcnt(0)
	v_mfma_f32_32x32x16_bf16 v[144:159], v[228:231], v[244:247], 0
	v_exp_f32_e32 v174, v174
	v_exp_f32_e32 v175, v175
	v_add_f32_e32 v15, v160, v161
	v_add_f32_e32 v211, v162, v163
	v_add_f32_e64 v15, v15, v211
	v_mfma_f32_32x32x16_bf16 v[144:159], v[232:235], v[248:251], v[144:159]
	v_add_f32_e32 v211, v164, v165
	v_add_f32_e32 v224, v166, v167
	v_add_f32_e32 v211, v211, v224
	v_add_f32_e32 v224, v168, v169
	v_add_f32_e32 v225, v170, v171
	v_add_f32_e32 v224, v224, v225
	v_add_f32_e32 v225, v172, v173
	v_add_f32_e32 v227, v174, v175
	v_add_f32_e32 v225, v225, v227
	v_add_f32_e32 v15, v15, v211
	v_add_f32_e64 v224, v224, v225
	v_mfma_f32_32x32x16_bf16 v[144:159], v[236:239], v[4:7], v[144:159]
	v_add_f32_e32 v15, v15, v224
	v_add_f32_e32 v207, v207, v15
	v_cvt_pk_bf16_f32 v160, v160, v161
	v_cvt_pk_bf16_f32 v161, v162, v163
	v_cvt_pk_bf16_f32 v162, v164, v165
	v_cvt_pk_bf16_f32 v163, v166, v167
	v_cvt_pk_bf16_f32 v164, v168, v169
	v_cvt_pk_bf16_f32 v165, v170, v171
	v_cvt_pk_bf16_f32 v166, v172, v173
	v_cvt_pk_bf16_f32 v167, v174, v175
	v_mfma_f32_32x32x16_bf16 v[144:159], v[240:243], v[8:11], v[144:159]
	s_nop 1
	s_nop 0
	v_mfma_f32_32x32x16_bf16 v[112:127], v[184:187], v[160:163], v[112:127]
	ds_read_b128 v[228:231], v12 offset:8832
	ds_read_b128 v[232:235], v12 offset:8864
	ds_read_b128 v[236:239], v12 offset:8896
	ds_read_b128 v[240:243], v12 offset:8928
	ds_read_b128 v[244:247], v13 offset:128
	ds_read_b128 v[248:251], v13 offset:160
	ds_read_b128 v[4:7], v13 offset:192
	ds_read_b128 v[8:11], v13 offset:224
	s_nop 3
	s_nop 0
	v_max3_f32 v15, v144, v145, v146
	v_max3_f32 v211, v147, v148, v149
	v_max3_f32 v224, v150, v151, v152
	v_mfma_f32_32x32x16_bf16 v[80:95], v[188:191], v[160:163], v[80:95]
	v_max3_f32 v225, v153, v154, v155
	v_max3_f32 v227, v156, v157, v158
	v_max3_f32 v15, v15, v211, v159
	v_max3_f32 v224, v224, v225, v227
	v_max_f32_e32 v15, v15, v224
	v_mov_b32_e32 v211, v15
	v_add_f32_e32 v225, 0x41000000, v209
	s_nop 1
	v_permlane32_swap_b32_e32 v15, v211
	v_max_f32_e32 v15, v15, v211
	v_cmp_gt_f32_e32 vcc, v15, v225
	s_cbranch_vccnz .Lat_slow0_s1
.Lat_back0_s1:
	s_nop 0
	v_mfma_f32_32x32x16_bf16 v[48:63], v[192:195], v[160:163], v[48:63]
	v_sub_f32_e32 v144, v144, v209
	v_sub_f32_e32 v145, v145, v209
	v_sub_f32_e32 v146, v146, v209
	v_sub_f32_e32 v147, v147, v209
	v_exp_f32_e32 v144, v144
	v_exp_f32_e32 v145, v145
	v_mfma_f32_32x32x16_bf16 v[16:31], v[196:199], v[160:163], v[16:31]
	v_exp_f32_e32 v146, v146
	v_exp_f32_e32 v147, v147
	v_sub_f32_e32 v148, v148, v209
	v_sub_f32_e32 v149, v149, v209
	v_sub_f32_e32 v150, v150, v209
	v_sub_f32_e32 v151, v151, v209
	v_mfma_f32_32x32x16_bf16 v[112:127], v[200:203], v[164:167], v[112:127]
	v_exp_f32_e32 v148, v148
	v_exp_f32_e32 v149, v149
	v_exp_f32_e64 v150, v150
	v_mfma_f32_32x32x16_bf16 v[80:95], v[212:215], v[164:167], v[80:95]
	v_exp_f32_e32 v151, v151
	v_sub_f32_e32 v152, v152, v209
	v_sub_f32_e32 v153, v153, v209
	v_sub_f32_e32 v154, v154, v209
	v_sub_f32_e32 v155, v155, v209
	v_exp_f32_e32 v152, v152
	v_mfma_f32_32x32x16_bf16 v[48:63], v[216:219], v[164:167], v[48:63]
	v_exp_f32_e32 v153, v153
	v_exp_f32_e32 v154, v154
	v_exp_f32_e64 v155, v155
	v_mfma_f32_32x32x16_bf16 v[16:31], v[220:223], v[164:167], v[16:31]
	v_sub_f32_e32 v156, v156, v209
	v_sub_f32_e32 v157, v157, v209
	v_sub_f32_e32 v158, v158, v209
	v_sub_f32_e32 v159, v159, v209
	v_exp_f32_e32 v156, v156
	v_exp_f32_e32 v157, v157
	ds_read_b128 v[184:187], v14 offset:34880
	ds_read_b128 v[188:191], v14 offset:39488
	ds_read_b128 v[192:195], v14 offset:44096
	ds_read_b128 v[196:199], v14 offset:48704
	ds_read_b128 v[200:203], v14 offset:34912
	ds_read_b128 v[212:215], v14 offset:39520
	ds_read_b128 v[216:219], v14 offset:44128
	s_waitcnt lgkmcnt(7)
	s_nop 0
	ds_read_b128 v[220:223], v14 offset:48736
	v_mfma_f32_32x32x16_bf16 v[160:175], v[228:231], v[244:247], 0
	v_exp_f32_e32 v158, v158
	v_exp_f32_e32 v159, v159
	v_add_f32_e32 v15, v144, v145
	v_add_f32_e32 v211, v146, v147
	v_add_f32_e64 v15, v15, v211
	v_mfma_f32_32x32x16_bf16 v[160:175], v[232:235], v[248:251], v[160:175]
	v_add_f32_e32 v211, v148, v149
	v_add_f32_e32 v224, v150, v151
	v_add_f32_e32 v211, v211, v224
	v_add_f32_e32 v224, v152, v153
	v_add_f32_e32 v225, v154, v155
	v_add_f32_e32 v224, v224, v225
	v_add_f32_e32 v225, v156, v157
	v_add_f32_e32 v227, v158, v159
	v_add_f32_e32 v225, v225, v227
	v_add_f32_e32 v15, v15, v211
	v_add_f32_e64 v224, v224, v225
	v_mfma_f32_32x32x16_bf16 v[160:175], v[236:239], v[4:7], v[160:175]
	v_add_f32_e32 v15, v15, v224
	v_add_f32_e32 v210, v210, v15
	v_cvt_pk_bf16_f32 v144, v144, v145
	v_cvt_pk_bf16_f32 v145, v146, v147
	v_cvt_pk_bf16_f32 v146, v148, v149
	v_cvt_pk_bf16_f32 v147, v150, v151
	v_cvt_pk_bf16_f32 v148, v152, v153
	v_cvt_pk_bf16_f32 v149, v154, v155
	v_cvt_pk_bf16_f32 v150, v156, v157
	v_cvt_pk_bf16_f32 v151, v158, v159
	v_mfma_f32_32x32x16_bf16 v[160:175], v[240:243], v[8:11], v[160:175]
	s_waitcnt lgkmcnt(0)
	s_nop 0
	v_mfma_f32_32x32x16_bf16 v[128:143], v[184:187], v[144:147], v[128:143]
	s_nop 11
	s_nop 0
	v_max3_f32 v15, v160, v161, v162
	v_max3_f32 v211, v163, v164, v165
	v_max3_f32 v224, v166, v167, v168
	v_max3_f32 v225, v169, v170, v171
	v_max3_f32 v227, v172, v173, v174
	v_max3_f32 v15, v15, v211, v175
	v_max3_f32 v224, v224, v225, v227
	v_max_f32_e32 v15, v15, v224
	v_mov_b32_e32 v211, v15
	v_add_f32_e32 v225, 0x41000000, v208
	s_nop 1
	v_permlane32_swap_b32_e32 v15, v211
	v_max_f32_e32 v15, v15, v211
	v_cmp_gt_f32_e32 vcc, v15, v225
	s_cbranch_vccnz .Lat_slow1_s1
.Lat_back1_s1:
	v_sub_f32_e32 v160, v160, v208
	v_sub_f32_e64 v161, v161, v208
	v_mfma_f32_32x32x16_bf16 v[96:111], v[188:191], v[144:147], v[96:111]
	v_sub_f32_e32 v162, v162, v208
	v_sub_f32_e32 v163, v163, v208
	v_exp_f32_e32 v160, v160
	v_exp_f32_e32 v161, v161
	v_exp_f32_e32 v162, v162
	v_exp_f32_e32 v163, v163
	v_mfma_f32_32x32x16_bf16 v[64:79], v[192:195], v[144:147], v[64:79]
	v_sub_f32_e32 v164, v164, v208
	v_sub_f32_e32 v165, v165, v208
	v_sub_f32_e32 v166, v166, v208
	v_sub_f32_e32 v167, v167, v208
	v_exp_f32_e32 v164, v164
	v_exp_f32_e32 v165, v165
	v_exp_f32_e64 v166, v166
	v_mfma_f32_32x32x16_bf16 v[32:47], v[196:199], v[144:147], v[32:47]
	v_exp_f32_e32 v167, v167
	v_sub_f32_e32 v168, v168, v208
	v_sub_f32_e32 v169, v169, v208
	v_sub_f32_e32 v170, v170, v208
	v_sub_f32_e32 v171, v171, v208
	v_exp_f32_e32 v168, v168
	v_exp_f32_e32 v169, v169
	v_exp_f32_e32 v170, v170
	v_mfma_f32_32x32x16_bf16 v[128:143], v[200:203], v[148:151], v[128:143]
	v_exp_f32_e32 v171, v171
	v_sub_f32_e32 v172, v172, v208
	v_sub_f32_e32 v173, v173, v208
	v_sub_f32_e32 v174, v174, v208
	v_sub_f32_e32 v175, v175, v208
	v_exp_f32_e32 v172, v172
	v_exp_f32_e64 v173, v173
	v_mfma_f32_32x32x16_bf16 v[96:111], v[212:215], v[148:151], v[96:111]
	v_exp_f32_e32 v174, v174
	v_exp_f32_e32 v175, v175
	v_add_f32_e32 v15, v160, v161
	v_add_f32_e32 v211, v162, v163
	v_add_f32_e32 v15, v15, v211
	v_add_f32_e32 v211, v164, v165
	v_add_f32_e32 v224, v166, v167
	v_add_f32_e32 v211, v211, v224
	v_add_f32_e64 v224, v168, v169
	v_mfma_f32_32x32x16_bf16 v[64:79], v[216:219], v[148:151], v[64:79]
	v_add_f32_e32 v225, v170, v171
	v_add_f32_e32 v224, v224, v225
	v_add_f32_e32 v225, v172, v173
	v_add_f32_e32 v227, v174, v175
	v_add_f32_e32 v225, v225, v227
	v_add_f32_e32 v15, v15, v211
	v_add_f32_e32 v224, v224, v225
	v_add_f32_e32 v15, v15, v224
	v_add_f32_e64 v207, v207, v15
	v_cvt_pk_bf16_f32 v160, v160, v161
	v_cvt_pk_bf16_f32 v161, v162, v163
	v_cvt_pk_bf16_f32 v162, v164, v165
	v_cvt_pk_bf16_f32 v163, v166, v167
	v_cvt_pk_bf16_f32 v164, v168, v169
	v_cvt_pk_bf16_f32 v165, v170, v171
	v_cvt_pk_bf16_f32 v166, v172, v173
	v_cvt_pk_bf16_f32 v167, v174, v175
	v_mfma_f32_32x32x16_bf16 v[32:47], v[220:223], v[148:151], v[32:47]
	s_nop 1
	s_nop 0
	v_mfma_f32_32x32x16_bf16 v[112:127], v[184:187], v[160:163], v[112:127]
	s_xor_b32 s8, s27, 1
	s_mulk_i32 s8, 0x4800
	s_waitcnt vmcnt(0)
	s_nop 0
	v_mfma_f32_32x32x16_bf16 v[80:95], v[188:191], v[160:163], v[80:95]
	v_add_u32_e64 v15, s8, v2
	ds_write_b16 v15, v176 offset:34816
	v_mfma_f32_32x32x16_bf16 v[48:63], v[192:195], v[160:163], v[48:63]
	ds_write_b16_d16_hi v15, v176 offset:34960
	ds_write_b16 v15, v177 offset:35104
	ds_write_b16_d16_hi v15, v177 offset:35248
	v_mfma_f32_32x32x16_bf16 v[16:31], v[196:199], v[160:163], v[16:31]
	ds_write_b16 v15, v178 offset:35392
	ds_write_b16_d16_hi v15, v178 offset:35536
	v_mfma_f32_32x32x16_bf16 v[112:127], v[200:203], v[164:167], v[112:127]
	ds_write_b16 v15, v179 offset:35680
	ds_write_b16_d16_hi v15, v179 offset:35824
	ds_write_b16 v15, v180 offset:44032
	v_mfma_f32_32x32x16_bf16 v[80:95], v[212:215], v[164:167], v[80:95]
	ds_write_b16_d16_hi v15, v180 offset:44176
	ds_write_b16 v15, v181 offset:44320
	v_mfma_f32_32x32x16_bf16 v[48:63], v[216:219], v[164:167], v[48:63]
	ds_write_b16_d16_hi v15, v181 offset:44464
	ds_write_b16 v15, v182 offset:44608
	ds_write_b16_d16_hi v15, v182 offset:44752
	v_mfma_f32_32x32x16_bf16 v[16:31], v[220:223], v[164:167], v[16:31]
	ds_write_b16 v15, v183 offset:44896
	ds_write_b16_d16_hi v15, v183 offset:45040
	s_add_i32 s23, s23, 64
	s_cmpk_lg_i32 s23, 0x1100
	s_waitcnt vmcnt(0) lgkmcnt(0)
	s_barrier
	s_cbranch_scc0 .Lat_exit
	s_mov_b32 s26, s25
	s_branch .LBB0_439
